# adds static priority 1 for waves 4-7 during the attention streams
# speedup vs baseline: 1.0089x; 1.0009x over previous
.LBB0_692:
	s_mov_b32 s77, s93
	s_add_i32 s58, s36, 0x3400
	s_add_i32 s59, s36, 0x2000
	s_add_i32 s38, s51, s83
	s_lshl_b64 s[8:9], s[76:77], 26
	s_add_u32 s39, s30, s8
	v_writelane_b32 v252, s40, 23
	s_addc_u32 s40, s28, s9
	s_add_u32 s41, s31, s8
	s_addc_u32 s42, s29, s9
	s_add_u32 s43, s35, s8
	s_addc_u32 s44, s34, s9
	s_add_u32 s45, s27, 0x80000
	s_addc_u32 s46, s26, 0
	s_add_u32 s47, s27, 0x3f200000
	s_addc_u32 s48, s26, 0
	s_add_i32 s49, s76, 1
	s_cmp_eq_u32 s76, 3
	s_mov_b32 s8, 0xa000
	s_cselect_b32 s50, 0x6000, s8
	s_lshl_b32 s61, s51, 5
	s_ashr_i32 s8, s61, 31
	s_add_u32 s22, s27, 0x1ae00000
	s_addc_u32 s23, s26, 0
	v_and_b32_e32 v204, 31, v2
	v_and_b32_e32 v9, 16, v2
	v_lshlrev_b32_e32 v10, 2, v2
	s_add_u32 s62, s27, 0x20e00000
	v_lshrrev_b32_e32 v5, 5, v4
	v_mul_u32_u24_e32 v6, 0xd0, v204
	v_lshlrev_b32_e32 v8, 4, v2
	v_and_or_b32 v9, v10, 12, v9
	s_addc_u32 s63, s26, 0
	v_lshl_add_u32 v205, v5, 4, v6
	v_lshlrev_b32_e32 v6, 8, v5
	v_and_b32_e32 v8, 0xc0, v8
	v_lshlrev_b32_e32 v9, 1, v9
	s_add_u32 s51, s27, 0x43200000
	v_and_b32_e32 v7, 15, v2
	v_or3_b32 v206, v6, v8, v9
	s_waitcnt vmcnt(6)
	s_barrier
	v_mov_b32_e32 v189, s8
	v_lshlrev_b32_e32 v6, 3, v5
	s_addc_u32 s52, s26, 0
	v_lshrrev_b32_e32 v2, 1, v2
	v_cmp_gt_u32_e64 s[8:9], 16, v4
	v_lshlrev_b32_e32 v8, 2, v5
	v_mov_b32_e32 v4, v3
	v_mov_b32_e32 v5, v3
	v_and_b32_e32 v178, 24, v2
	s_add_u32 s24, s27, 0x2f200000
	v_mov_b32_e32 v2, v3
	v_mov_b64_e32 v[100:101], v[4:5]
	s_mov_b32 s60, 3
	v_or_b32_e32 v188, s61, v204
	v_lshlrev_b32_e32 v199, 11, v7
	v_mov_b32_e32 v179, v3
	v_lshlrev_b32_e32 v180, 2, v7
	s_addc_u32 s25, s26, 0
	v_or_b32_e32 v207, 59, v8
	v_mov_b32_e32 v102, v3
	v_mov_b32_e32 v103, v3
	v_mov_b32_e32 v104, v3
	v_mov_b32_e32 v105, v3
	v_mov_b32_e32 v106, v3
	v_mov_b32_e32 v107, v3
	v_mov_b32_e32 v108, v3
	v_mov_b32_e32 v109, v3
	v_mov_b32_e32 v110, v3
	v_mov_b32_e32 v111, v3
	v_mov_b32_e32 v112, v3
	v_mov_b32_e32 v113, v3
	v_mov_b32_e32 v114, v3
	v_mov_b32_e32 v115, v3
	v_mov_b32_e32 v116, v3
	v_mov_b32_e32 v117, v3
	v_mov_b32_e32 v118, v3
	v_mov_b32_e32 v119, v3
	v_mov_b32_e32 v120, v3
	v_mov_b32_e32 v121, v3
	v_mov_b32_e32 v122, v3
	v_mov_b32_e32 v123, v3
	v_mov_b32_e32 v124, v3
	v_mov_b32_e32 v125, v3
	v_mov_b32_e32 v126, v3
	v_mov_b32_e32 v127, v3
	v_mov_b32_e32 v128, v3
	v_mov_b32_e32 v129, v3
	v_mov_b32_e32 v130, v3
	v_mov_b32_e32 v131, v3
	v_mov_b32_e32 v132, v3
	v_mov_b32_e32 v133, v3
	v_mov_b64_e32 v[186:187], 0
	s_mov_b32 s64, 0
	v_lshlrev_b32_e32 v190, 1, v6
	v_lshlrev_b32_e32 v192, 1, v8
	v_readlane_b32 s65, v252, 28
	v_readlane_b32 s66, v252, 26
	v_readlane_b32 s67, v252, 18
	s_mov_b32 s69, 0
	s_mov_b32 s70, 0
	v_mov_b64_e32 v[98:99], v[2:3]
	v_mov_b64_e32 v[184:185], 0
	v_mov_b64_e32 v[182:183], 0
	s_mov_b32 s68, 0
	s_mov_b32 s53, 0
	s_cmp_lt_u32 s61, 0x80
	s_cbranch_scc1 .Lprio_skip
	s_setprio 1
.Lprio_skip:
.LBB0_693:
	s_lshl_b32 s10, s66, 12
	s_ashr_i32 s11, s67, 31
	s_add_u32 s10, s67, s10
	s_addc_u32 s11, s11, 0
	v_lshl_add_u64 v[202:203], s[10:11], 0, v[188:189]
	v_mov_b64_e32 v[4:5], s[22:23]
	s_movk_i32 s26, 0x600
	v_mad_u64_u32 v[4:5], s[10:11], v202, s26, v[4:5]
	v_mov_b32_e32 v2, v5
	v_mad_u64_u32 v[6:7], s[10:11], v203, s26, v[2:3]
	v_mov_b32_e32 v5, v6
	s_mul_i32 s92, s65, 0x60
	v_lshl_add_u64 v[4:5], s[92:93], 1, v[4:5]
	v_mov_b32_e32 v191, v3
	v_lshl_add_u64 v[4:5], v[4:5], 0, v[190:191]
	global_load_dwordx4 v[134:137], v[4:5], off
	global_load_dwordx4 v[138:141], v[4:5], off offset:32
	global_load_dwordx4 v[142:145], v[4:5], off offset:64
	global_load_dwordx4 v[146:149], v[4:5], off offset:96
	global_load_dwordx4 v[150:153], v[4:5], off offset:128
	global_load_dwordx4 v[154:157], v[4:5], off offset:160
	s_add_i32 s72, s67, s61
	s_cmp_lt_i32 s72, 64
	s_waitcnt vmcnt(0)
	s_cbranch_scc1 .LBB0_740
	s_ashr_i32 s10, s72, 31
	s_lshr_b32 s10, s10, 26
	v_mov_b32_e32 v16, v3
	v_mov_b32_e32 v17, v3
	s_add_i32 s10, s72, s10
	v_mov_b32_e32 v2, v3
	v_mov_b32_e32 v4, v3
	v_mov_b32_e32 v5, v3
	v_mov_b32_e32 v6, v3
	v_mov_b32_e32 v7, v3
	v_mov_b32_e32 v8, v3
	v_mov_b32_e32 v9, v3
	v_mov_b32_e32 v10, v3
	v_mov_b32_e32 v11, v3
	v_mov_b32_e32 v12, v3
	v_mov_b32_e32 v13, v3
	v_mov_b32_e32 v14, v3
	v_mov_b32_e32 v15, v3
	v_mov_b32_e32 v191, 0
	v_mov_b64_e32 v[48:49], v[16:17]
	v_mov_b64_e32 v[32:33], v[16:17]
	s_ashr_i32 s71, s10, 6
	s_mov_b32 s73, 0
	v_mov_b64_e32 v[46:47], v[14:15]
	v_mov_b64_e32 v[44:45], v[12:13]
	v_mov_b64_e32 v[42:43], v[10:11]
	v_mov_b64_e32 v[40:41], v[8:9]
	v_mov_b64_e32 v[38:39], v[6:7]
	v_mov_b64_e32 v[36:37], v[4:5]
	v_mov_b64_e32 v[34:35], v[2:3]
	v_mov_b64_e32 v[30:31], v[14:15]
	v_mov_b64_e32 v[28:29], v[12:13]
	v_mov_b64_e32 v[26:27], v[10:11]
	v_mov_b64_e32 v[24:25], v[8:9]
	v_mov_b64_e32 v[22:23], v[6:7]
	v_mov_b64_e32 v[20:21], v[4:5]
	v_mov_b64_e32 v[18:19], v[2:3]
	v_mov_b32_e32 v193, 0
	v_mov_b32_e32 v50, 0
	v_mov_b32_e32 v51, v191
	v_mov_b32_e32 v52, v191
	v_mov_b32_e32 v53, v191
	v_mov_b32_e32 v54, v191
	v_mov_b32_e32 v55, v191
	v_mov_b32_e32 v56, v191
	v_mov_b32_e32 v57, v191
	v_mov_b32_e32 v58, v191
	v_mov_b32_e32 v59, v191
	v_mov_b32_e32 v60, v191
	v_mov_b32_e32 v61, v191
	v_mov_b32_e32 v62, v191
	v_mov_b32_e32 v63, v191
	v_mov_b32_e32 v64, v191
	v_mov_b32_e32 v65, v191
	s_branch .LBB0_696

.LBB0_915:
	s_setprio 0
	v_readlane_b32 s0, v255, 26
	s_add_i32 s33, s0, 4
	s_cmp_ge_i32 s33, s73
	s_cbranch_scc1 .LBB0_961
	s_waitcnt vmcnt(0)
	s_barrier
	s_and_saveexec_b64 s[30:31], s[90:91]
	s_cbranch_execz .LBB0_960
	v_readlane_b32 s0, v254, 15
	s_waitcnt vmcnt(0) expcnt(0) lgkmcnt(0)
	s_nop 0
	v_mov_b32_e32 v1, s0
	v_readlane_b32 s0, v254, 16
	ds_read_b32 v5, v1
	s_nop 0
	v_mov_b32_e32 v1, s0
	v_readlane_b32 s0, v254, 17
	ds_read_b32 v4, v1
	s_nop 0
	v_mov_b32_e32 v1, s0
	v_readlane_b32 s0, v254, 18
	ds_read_b32 v1, v1
	s_waitcnt lgkmcnt(0)
	v_readfirstlane_b32 s34, v1
	v_mov_b32_e32 v2, s0
	ds_read_b32 v6, v2
	v_readlane_b32 s0, v254, 19
	s_waitcnt lgkmcnt(0)
	v_cmp_ne_u32_e32 vcc, 0, v6
	v_mov_b32_e32 v2, s0
	ds_read_b32 v2, v2
	s_cbranch_vccnz .LBB0_931
	s_load_dwordx2 s[0:1], s[96:97], 0x4
	s_mov_b64 s[2:3], 0x1000
	v_lshl_add_u64 v[6:7], v[4:5], 0, s[2:3]
	s_mov_b64 s[2:3], 0x1100
	v_lshl_add_u64 v[8:9], v[4:5], 0, s[2:3]
	s_mov_b64 s[2:3], 0x1200
	v_lshl_add_u64 v[10:11], v[4:5], 0, s[2:3]
	s_mov_b64 s[2:3], 0x1300
	s_waitcnt lgkmcnt(0)
	s_mul_i32 s18, s0, s78
	v_lshl_add_u64 v[12:13], v[4:5], 0, s[2:3]
	s_mul_i32 s18, s18, s1
	s_mov_b32 s19, 1
	s_mov_b64 s[0:1], 0
	s_branch .LBB0_921
